# L0 rwkv yfin job loop: all 56 MFMA-part loads issued at job top into spare VGPRs, epilogue row loads and ln_x params issued once per job
# speedup vs baseline: 1.0005x; 1.0005x over previous
.LBB0_1417:
	s_ashr_i32 s0, s10, 31
	s_lshr_b32 s0, s0, 25
	s_add_i32 s4, s10, s0
	s_and_b32 s2, s4, 0xffffff80
	s_sub_i32 s0, s10, s2
	s_add_i32 s2, s10, s2
	s_ashr_i32 s3, s2, 31
	s_lshl_b64 s[8:9], s[2:3], 13
	v_lshl_add_u64 v[14:15], v[34:35], 0, s[8:9]
	s_lshl_b64 s[8:9], s[2:3], 12
	v_lshl_add_u64 v[100:101], v[48:49], 0, s[8:9]
	v_lshl_add_u64 v[108:109], v[52:53], 0, s[8:9]
	v_readfirstlane_b32 s8, v14
	v_readfirstlane_b32 s9, v15
	global_load_dwordx4 v[2:5], v[100:101], off
	global_load_dwordx4 v[6:9], v[100:101], off offset:1024
	global_load_dwordx2 v[12:13], v[108:109], off
	s_nop 1
	global_load_dwordx2 v[14:15], v45, s[8:9]
	global_load_dwordx2 v[16:17], v45, s[8:9] offset:512
	global_load_dwordx2 v[56:57], v45, s[8:9] offset:1024
	global_load_dwordx2 v[58:59], v45, s[8:9] offset:1536
	global_load_dwordx2 v[62:63], v[108:109], off offset:512
	global_load_dwordx2 v[72:73], v45, s[8:9] offset:2048
	global_load_dwordx2 v[74:75], v45, s[8:9] offset:2560
	global_load_dwordx2 v[76:77], v45, s[8:9] offset:3072
	global_load_dwordx2 v[78:79], v45, s[8:9] offset:3584
	global_load_dwordx2 v[82:83], v[108:109], off offset:1024
	global_load_dwordx2 v[84:85], v47, s[8:9]
	global_load_dwordx2 v[86:87], v47, s[8:9] offset:512
	global_load_dwordx2 v[88:89], v64, s[8:9]
	global_load_dwordx2 v[90:91], v64, s[8:9] offset:512
	global_load_dwordx2 v[94:95], v[108:109], off offset:1536
	global_load_dwordx2 v[96:97], v43, s[8:9]
	global_load_dwordx2 v[98:99], v43, s[8:9] offset:512
	global_load_dwordx2 v[174:175], v65, s[8:9]
	global_load_dwordx2 v[176:177], v65, s[8:9] offset:512
	global_load_dwordx4 v[150:153], v[100:101], off offset:2048
	global_load_dwordx4 v[154:157], v[100:101], off offset:3072
	global_load_dwordx2 v[178:179], v[108:109], off offset:2048
	global_load_dwordx2 v[180:181], v[108:109], off offset:2560
	global_load_dwordx2 v[182:183], v[108:109], off offset:3072
	global_load_dwordx2 v[184:185], v[108:109], off offset:3584
	s_addk_i32 s2, 0x80
	s_ashr_i32 s3, s2, 31
	s_lshl_b64 s[8:9], s[2:3], 12
	v_lshl_add_u64 v[132:133], v[32:33], 0, s[8:9]
	v_lshl_add_u64 v[128:129], v[50:51], 0, s[8:9]
	v_lshl_add_u64 v[134:135], v[54:55], 1, v[132:133]
	s_lshl_b64 s[2:3], s[2:3], 13
	v_lshl_add_u64 v[144:145], v[34:35], 0, s[2:3]
	v_readfirstlane_b32 s8, v132
	v_readfirstlane_b32 s9, v133
	v_readfirstlane_b32 s2, v144
	v_readfirstlane_b32 s3, v145
	s_nop 4
	global_load_dwordx4 v[158:161], v[128:129], off offset:2048
	global_load_dwordx4 v[162:165], v[128:129], off offset:3072
	global_load_dwordx2 v[186:187], v[134:135], off offset:2048
	global_load_dwordx2 v[188:189], v45, s[2:3]
	global_load_dwordx2 v[190:191], v45, s[2:3] offset:512
	global_load_dwordx2 v[192:193], v45, s[2:3] offset:1024
	global_load_dwordx2 v[194:195], v45, s[2:3] offset:1536
	global_load_dwordx2 v[196:197], v[134:135], off offset:2560
	global_load_dwordx2 v[198:199], v45, s[2:3] offset:2048
	global_load_dwordx2 v[200:201], v45, s[2:3] offset:2560
	global_load_dwordx2 v[202:203], v45, s[2:3] offset:3072
	global_load_dwordx2 v[204:205], v45, s[2:3] offset:3584
	global_load_dwordx2 v[206:207], v[134:135], off offset:3072
	global_load_dwordx2 v[208:209], v47, s[2:3]
	global_load_dwordx2 v[210:211], v47, s[2:3] offset:512
	global_load_dwordx2 v[212:213], v64, s[2:3]
	global_load_dwordx2 v[214:215], v64, s[2:3] offset:512
	global_load_dwordx2 v[216:217], v[134:135], off offset:3584
	global_load_dwordx2 v[218:219], v43, s[2:3]
	global_load_dwordx2 v[220:221], v43, s[2:3] offset:512
	global_load_dwordx2 v[222:223], v65, s[2:3]
	global_load_dwordx2 v[136:137], v65, s[2:3] offset:512
	global_load_dwordx4 v[166:169], v[128:129], off
	global_load_dwordx4 v[170:173], v[128:129], off offset:1024
	global_load_dwordx2 v[138:139], v[134:135], off offset:1024
	global_load_dwordx2 v[140:141], v[134:135], off offset:512
	global_load_dwordx2 v[230:231], v66, s[8:9]
	global_load_dwordx2 v[238:239], v[134:135], off offset:1536
	s_ashr_i32 s6, s4, 10
	s_ashr_i32 s7, s6, 31
	s_ashr_i32 s1, s0, 31
	s_lshl_b64 s[0:1], s[0:1], 5
	s_lshl_b64 s[6:7], s[6:7], 12
	v_add_u32_e32 v38, 0x1000, v67
	s_waitcnt vmcnt(53)
	v_lshlrev_b32_e32 v10, 16, v12
	v_and_b32_e32 v11, 0xffff0000, v12
	v_lshlrev_b32_e32 v12, 16, v13
	v_and_b32_e32 v13, 0xffff0000, v13
	s_waitcnt vmcnt(48)
	v_lshlrev_b32_e32 v60, 16, v62
	v_and_b32_e32 v61, 0xffff0000, v62
	v_lshlrev_b32_e32 v62, 16, v63
	v_and_b32_e32 v63, 0xffff0000, v63
	s_waitcnt vmcnt(43)
	v_lshlrev_b32_e32 v80, 16, v82
	v_and_b32_e32 v81, 0xffff0000, v82
	v_lshlrev_b32_e32 v82, 16, v83
	v_and_b32_e32 v83, 0xffff0000, v83
	s_waitcnt vmcnt(38)
	v_lshlrev_b32_e32 v92, 16, v94
	v_and_b32_e32 v93, 0xffff0000, v94
	v_lshlrev_b32_e32 v94, 16, v95
	v_and_b32_e32 v95, 0xffff0000, v95
	v_mfma_f32_16x16x32_bf16 v[10:13], v[2:5], v[14:17], v[10:13]
	v_mfma_f32_16x16x32_bf16 v[60:63], v[2:5], v[72:75], v[60:63]
	v_mfma_f32_16x16x32_bf16 v[80:83], v[2:5], v[84:87], v[80:83]
	s_waitcnt vmcnt(36)
	v_mfma_f32_16x16x32_bf16 v[2:5], v[2:5], v[96:99], v[92:95]
	s_nop 2
	s_nop 5
	s_waitcnt vmcnt(35)
	v_mov_b64 v[92:93], v[174:175]
	s_nop 1
	s_waitcnt vmcnt(34)
	v_mov_b64 v[94:95], v[176:177]
	s_nop 1
	v_mfma_f32_16x16x32_bf16 v[10:13], v[6:9], v[56:59], v[10:13]
	v_mfma_f32_16x16x32_bf16 v[60:63], v[6:9], v[76:79], v[60:63]
	s_add_u32 s13, s6, s0
	s_addc_u32 s14, s7, s1
	s_lshr_b32 s0, s4, 1
	v_mfma_f32_16x16x32_bf16 v[80:83], v[6:9], v[88:91], v[80:83]
	s_and_b32 s12, s0, 0x1c0
	v_readfirstlane_b32 s6, v18
	v_readfirstlane_b32 s7, v19
	v_readfirstlane_b32 s8, v20
	v_readfirstlane_b32 s9, v21
	s_lshl_b32 s4, s12, 1
	s_add_i32 s10, s10, s94
	s_cmpk_lt_i32 s10, 0x1000
	v_mfma_f32_16x16x32_bf16 v[2:5], v[6:9], v[92:95], v[2:5]
	s_nop 8
	s_waitcnt vmcnt(33)
	v_mov_b64 v[6:7], v[150:151]
	v_mov_b64 v[8:9], v[152:153]
	s_nop 1
	s_nop 0
	s_waitcnt vmcnt(32)
	v_mov_b64 v[100:101], v[154:155]
	v_mov_b64 v[102:103], v[156:157]
	s_nop 1
	s_nop 0
	s_waitcnt vmcnt(31)
	v_mov_b64 v[106:107], v[178:179]
	s_nop 1
	v_lshlrev_b32_e32 v104, 16, v106
	v_and_b32_e32 v105, 0xffff0000, v106
	v_lshlrev_b32_e32 v106, 16, v107
	v_and_b32_e32 v107, 0xffff0000, v107
	s_nop 1
	v_mfma_f32_16x16x32_bf16 v[14:17], v[6:9], v[14:17], v[104:107]
	v_mfma_f32_16x16x32_bf16 v[14:17], v[100:103], v[56:59], v[14:17]
	s_nop 8
	s_waitcnt vmcnt(30)
	v_mov_b64 v[58:59], v[180:181]
	s_nop 1
	v_lshlrev_b32_e32 v56, 16, v58
	v_and_b32_e32 v57, 0xffff0000, v58
	v_lshlrev_b32_e32 v58, 16, v59
	v_and_b32_e32 v59, 0xffff0000, v59
	s_nop 1
	v_mfma_f32_16x16x32_bf16 v[56:59], v[6:9], v[72:75], v[56:59]
	s_nop 8
	s_waitcnt vmcnt(29)
	v_mov_b64 v[74:75], v[182:183]
	s_nop 1
	v_mfma_f32_16x16x32_bf16 v[56:59], v[100:103], v[76:79], v[56:59]
	s_nop 8
	s_waitcnt vmcnt(28)
	v_mov_b64 v[78:79], v[184:185]
	s_nop 1
	v_lshlrev_b32_e32 v72, 16, v74
	v_and_b32_e32 v73, 0xffff0000, v74
	v_lshlrev_b32_e32 v74, 16, v75
	v_and_b32_e32 v75, 0xffff0000, v75
	v_lshlrev_b32_e32 v76, 16, v78
	v_and_b32_e32 v77, 0xffff0000, v78
	v_lshlrev_b32_e32 v78, 16, v79
	v_and_b32_e32 v79, 0xffff0000, v79
	v_mfma_f32_16x16x32_bf16 v[72:75], v[6:9], v[84:87], v[72:75]
	s_nop 0
	v_mfma_f32_16x16x32_bf16 v[6:9], v[6:9], v[96:99], v[76:79]
	v_mfma_f32_16x16x32_bf16 v[72:75], v[100:103], v[88:91], v[72:75]
	s_nop 0
	v_mfma_f32_16x16x32_bf16 v[76:79], v[100:103], v[92:95], v[6:9]
	s_nop 2
	s_nop 5
	s_waitcnt vmcnt(27)
	v_mov_b64 v[6:7], v[158:159]
	v_mov_b64 v[8:9], v[160:161]
	s_nop 1
	s_waitcnt vmcnt(26)
	v_mov_b64 v[84:85], v[162:163]
	v_mov_b64 v[86:87], v[164:165]
	s_nop 1
	s_waitcnt vmcnt(25)
	v_mov_b64 v[90:91], v[186:187]
	s_nop 1
	v_and_b32_e32 v92, 0xffff0000, v91
	v_lshlrev_b32_e32 v93, 16, v91
	v_pk_add_f32 v[10:11], v[10:11], v[92:93]
	v_and_b32_e32 v92, 0xffff0000, v90
	v_lshlrev_b32_e32 v93, 16, v90
	s_waitcnt vmcnt(24)
	v_mov_b64 v[88:89], v[188:189]
	s_nop 1
	s_waitcnt vmcnt(23)
	v_mov_b64 v[90:91], v[190:191]
	s_nop 1
	v_pk_add_f32 v[12:13], v[12:13], v[92:93]
	s_waitcnt vmcnt(22)
	v_mov_b64 v[92:93], v[192:193]
	s_nop 1
	s_waitcnt vmcnt(21)
	v_mov_b64 v[94:95], v[194:195]
	s_nop 1
	v_mfma_f32_16x16x32_bf16 v[10:13], v[6:9], v[88:91], v[10:13]
	v_mfma_f32_16x16x32_bf16 v[96:99], v[84:87], v[92:95], v[10:13]
	s_nop 5
	s_nop 2
	s_waitcnt vmcnt(20)
	v_mov_b64 v[12:13], v[196:197]
	s_nop 1
	v_and_b32_e32 v10, 0xffff0000, v13
	v_lshlrev_b32_e32 v11, 16, v13
	v_pk_add_f32 v[10:11], v[60:61], v[10:11]
	v_and_b32_e32 v60, 0xffff0000, v12
	v_lshlrev_b32_e32 v61, 16, v12
	v_pk_add_f32 v[12:13], v[62:63], v[60:61]
	s_waitcnt vmcnt(19)
	v_mov_b64 v[60:61], v[198:199]
	s_nop 1
	s_waitcnt vmcnt(18)
	v_mov_b64 v[62:63], v[200:201]
	s_nop 1
	s_waitcnt vmcnt(17)
	v_mov_b64 v[100:101], v[202:203]
	s_nop 1
	s_waitcnt vmcnt(16)
	v_mov_b64 v[102:103], v[204:205]
	s_nop 1
	v_mfma_f32_16x16x32_bf16 v[10:13], v[6:9], v[60:63], v[10:13]
	v_mfma_f32_16x16x32_bf16 v[104:107], v[84:87], v[100:103], v[10:13]
	s_nop 5
	s_nop 2
	s_waitcnt vmcnt(15)
	v_mov_b64 v[12:13], v[206:207]
	s_nop 1
	v_and_b32_e32 v10, 0xffff0000, v13
	v_lshlrev_b32_e32 v11, 16, v13
	v_pk_add_f32 v[10:11], v[80:81], v[10:11]
	v_and_b32_e32 v80, 0xffff0000, v12
	v_lshlrev_b32_e32 v81, 16, v12
	v_pk_add_f32 v[12:13], v[82:83], v[80:81]
	s_waitcnt vmcnt(14)
	v_mov_b64 v[80:81], v[208:209]
	s_nop 1
	s_waitcnt vmcnt(13)
	v_mov_b64 v[82:83], v[210:211]
	s_nop 1
	s_waitcnt vmcnt(12)
	v_mov_b64 v[108:109], v[212:213]
	s_nop 1
	s_waitcnt vmcnt(11)
	v_mov_b64 v[110:111], v[214:215]
	s_nop 1
	v_mfma_f32_16x16x32_bf16 v[10:13], v[6:9], v[80:83], v[10:13]
	v_mfma_f32_16x16x32_bf16 v[112:115], v[84:87], v[108:111], v[10:13]
	s_nop 5
	s_nop 2
	s_waitcnt vmcnt(10)
	v_mov_b64 v[10:11], v[216:217]
	s_nop 1
	s_waitcnt vmcnt(9)
	v_mov_b64 v[116:117], v[218:219]
	s_nop 1
	s_waitcnt vmcnt(8)
	v_mov_b64 v[118:119], v[220:221]
	s_nop 1
	s_waitcnt vmcnt(7)
	v_mov_b64 v[120:121], v[222:223]
	s_nop 1
	s_waitcnt vmcnt(6)
	v_mov_b64 v[122:123], v[136:137]
	s_nop 1
	s_waitcnt vmcnt(5)
	v_mov_b64 v[124:125], v[166:167]
	v_mov_b64 v[126:127], v[168:169]
	s_nop 1
	s_nop 0
	s_waitcnt vmcnt(4)
	v_mov_b64 v[128:129], v[170:171]
	v_mov_b64 v[130:131], v[172:173]
	s_nop 1
	v_and_b32_e32 v12, 0xffff0000, v11
	v_lshlrev_b32_e32 v13, 16, v11
	v_pk_add_f32 v[2:3], v[2:3], v[12:13]
	v_and_b32_e32 v12, 0xffff0000, v10
	v_lshlrev_b32_e32 v13, 16, v10
	v_pk_add_f32 v[4:5], v[4:5], v[12:13]
	s_waitcnt vmcnt(3)
	v_mov_b64 v[12:13], v[138:139]
	s_nop 1
	v_mfma_f32_16x16x32_bf16 v[2:5], v[6:9], v[116:119], v[2:5]
	s_nop 8
	s_waitcnt vmcnt(2)
	v_mov_b64 v[8:9], v[140:141]
	s_nop 1
	v_and_b32_e32 v10, 0xffff0000, v8
	v_mfma_f32_16x16x32_bf16 v[84:87], v[84:87], v[120:123], v[2:5]
	v_lshlrev_b32_e32 v11, 16, v8
	s_nop 2
	s_nop 4
	s_waitcnt vmcnt(1)
	v_mov_b64 v[4:5], v[230:231]
	s_nop 1
	v_and_b32_e32 v6, 0xffff0000, v4
	v_lshlrev_b32_e32 v7, 16, v4
	v_and_b32_e32 v2, 0xffff0000, v5
	v_lshlrev_b32_e32 v3, 16, v5
	v_pk_add_f32 v[4:5], v[16:17], v[6:7]
	s_waitcnt vmcnt(0)
	v_mov_b64 v[16:17], v[238:239]
	s_nop 1
	v_mov_b32_e32 v137, s14
	v_or_b32_e32 v136, s13, v40
	v_lshlrev_b64 v[136:137], 9, v[136:137]
	v_or_b32_e32 v136, v136, v36
	v_or_b32_e32 v136, s12, v136
	v_lshlrev_b64 v[136:137], 1, v[136:137]
	v_lshl_add_u64 v[138:139], v[24:25], 0, v[136:137]
	global_load_dwordx4 v[150:153], v[138:139], off
	v_lshl_add_u64 v[138:139], v[26:27], 0, v[136:137]
	global_load_dwordx4 v[154:157], v[138:139], off
	v_lshl_add_u64 v[138:139], v[28:29], 0, v[136:137]
	global_load_dwordx4 v[158:161], v[138:139], off
	v_lshl_add_u64 v[138:139], v[30:31], 0, v[136:137]
	global_load_dwordx4 v[162:165], v[138:139], off
	v_or_b32_e32 v140, s12, v36
	v_lshlrev_b32_e32 v140, 2, v140
	global_load_dwordx4 v[198:201], v140, s[6:7] offset:16
	global_load_dwordx4 v[202:205], v140, s[6:7]
	global_load_dwordx4 v[206:209], v140, s[8:9] offset:16
	global_load_dwordx4 v[210:213], v140, s[8:9]
	v_mov_b32_e32 v137, s14
	v_or_b32_e32 v136, s13, v42
	v_lshlrev_b64 v[136:137], 9, v[136:137]
	v_or_b32_e32 v136, v136, v36
	v_or_b32_e32 v136, s12, v136
	v_lshlrev_b64 v[136:137], 1, v[136:137]
	v_lshl_add_u64 v[138:139], v[24:25], 0, v[136:137]
	global_load_dwordx4 v[166:169], v[138:139], off
	v_lshl_add_u64 v[138:139], v[26:27], 0, v[136:137]
	global_load_dwordx4 v[170:173], v[138:139], off
	v_lshl_add_u64 v[138:139], v[28:29], 0, v[136:137]
	global_load_dwordx4 v[174:177], v[138:139], off
	v_lshl_add_u64 v[138:139], v[30:31], 0, v[136:137]
	global_load_dwordx4 v[178:181], v[138:139], off
	v_mov_b32_e32 v137, s14
	v_or_b32_e32 v136, s13, v44
	v_lshlrev_b64 v[136:137], 9, v[136:137]
	v_or_b32_e32 v136, v136, v36
	v_or_b32_e32 v136, s12, v136
	v_lshlrev_b64 v[136:137], 1, v[136:137]
	v_lshl_add_u64 v[138:139], v[24:25], 0, v[136:137]
	global_load_dwordx4 v[182:185], v[138:139], off
	v_lshl_add_u64 v[138:139], v[26:27], 0, v[136:137]
	global_load_dwordx4 v[186:189], v[138:139], off
	v_lshl_add_u64 v[138:139], v[28:29], 0, v[136:137]
	global_load_dwordx4 v[190:193], v[138:139], off
	v_lshl_add_u64 v[138:139], v[30:31], 0, v[136:137]
	global_load_dwordx4 v[194:197], v[138:139], off
	v_and_b32_e32 v6, 0xffff0000, v9
	v_lshlrev_b32_e32 v7, 16, v9
	v_pk_add_f32 v[2:3], v[14:15], v[2:3]
	v_pk_add_f32 v[6:7], v[56:57], v[6:7]
	v_pk_add_f32 v[8:9], v[58:59], v[10:11]
	v_and_b32_e32 v14, 0xffff0000, v12
	v_lshlrev_b32_e32 v15, 16, v12
	v_mfma_f32_16x16x32_bf16 v[2:5], v[124:127], v[88:91], v[2:5]
	v_and_b32_e32 v10, 0xffff0000, v13
	v_lshlrev_b32_e32 v11, 16, v13
	v_pk_add_f32 v[12:13], v[74:75], v[14:15]
	v_mfma_f32_16x16x32_bf16 v[6:9], v[124:127], v[60:63], v[6:9]
	v_add_f32_e64 v10, v72, v10
	v_add_f32_e64 v11, v73, v11
	ds_write2_b32 v67, v96, v104 offset1:16
	ds_write2_b32 v67, v97, v105 offset0:68 offset1:84
	ds_write2_b32 v67, v98, v106 offset0:136 offset1:152
	ds_write2_b32 v67, v99, v107 offset0:204 offset1:220
	ds_write2_b32 v67, v112, v84 offset0:32 offset1:48
	ds_write2_b32 v67, v113, v85 offset0:100 offset1:116
	ds_write2_b32 v67, v114, v86 offset0:168 offset1:184
	ds_write2_b32 v67, v115, v87 offset0:236 offset1:252
	v_and_b32_e32 v14, 0xffff0000, v17
	v_lshlrev_b32_e32 v15, 16, v17
	v_and_b32_e32 v56, 0xffff0000, v16
	v_lshlrev_b32_e32 v57, 16, v16
	v_pk_add_f32 v[14:15], v[76:77], v[14:15]
	v_pk_add_f32 v[16:17], v[78:79], v[56:57]
	v_mfma_f32_16x16x32_bf16 v[10:13], v[124:127], v[80:83], v[10:13]
	s_nop 0
	v_mfma_f32_16x16x32_bf16 v[14:17], v[124:127], v[116:119], v[14:17]
	v_mfma_f32_16x16x32_bf16 v[2:5], v[128:131], v[92:95], v[2:5]
	v_mfma_f32_16x16x32_bf16 v[6:9], v[128:131], v[100:103], v[6:9]
	s_nop 7
	ds_write2_b32 v38, v2, v6 offset0:64 offset1:80
	ds_write2_b32 v38, v3, v7 offset0:132 offset1:148
	ds_write2_b32 v38, v4, v8 offset0:200 offset1:216
	v_mfma_f32_16x16x32_bf16 v[10:13], v[128:131], v[108:111], v[10:13]
	v_add_u32_e32 v2, 0x1400, v67
	v_mfma_f32_16x16x32_bf16 v[14:17], v[128:131], v[120:123], v[14:17]
	ds_write2_b32 v2, v5, v9 offset0:12 offset1:28
	s_nop 6
	ds_write2_b32 v38, v10, v14 offset0:96 offset1:112
	ds_write2_b32 v38, v11, v15 offset0:164 offset1:180
	ds_write2_b32 v38, v12, v16 offset0:232 offset1:248
	ds_write2_b32 v2, v13, v17 offset0:44 offset1:60
	v_mov_b32_e32 v15, s14
	v_or_b32_e32 v14, s13, v40
	v_lshlrev_b64 v[6:7], 9, v[14:15]
	v_or_b32_e32 v2, v6, v36
	v_or_b32_e32 v6, s12, v2
	v_lshlrev_b64 v[10:11], 1, v[6:7]
	s_waitcnt lgkmcnt(0)
	v_lshl_add_u64 v[6:7], v[24:25], 0, v[10:11]
	ds_read_b128 v[2:5], v68
	ds_read_b128 v[72:75], v68 offset:16
	s_waitcnt vmcnt(15)
	v_mov_b64 v[56:57], v[150:151]
	v_mov_b64 v[58:59], v[152:153]
	s_nop 1
	v_lshl_add_u64 v[6:7], v[26:27], 0, v[10:11]
	s_waitcnt vmcnt(14)
	v_mov_b64 v[60:61], v[154:155]
	v_mov_b64 v[62:63], v[156:157]
	s_nop 1
	v_or_b32_e32 v16, s12, v36
	v_lshl_add_u64 v[6:7], v[28:29], 0, v[10:11]
	v_lshl_add_u64 v[10:11], v[30:31], 0, v[10:11]
	v_lshlrev_b32_e32 v17, 2, v16
	s_waitcnt vmcnt(13)
	v_mov_b64 v[6:7], v[158:159]
	v_mov_b64 v[8:9], v[160:161]
	s_nop 1
	s_waitcnt lgkmcnt(1)
	v_add_f32_e32 v38, 0, v2
	s_waitcnt vmcnt(12)
	v_mov_b64 v[10:11], v[162:163]
	v_mov_b64 v[12:13], v[164:165]
	s_nop 1
	v_add_f32_e32 v16, v3, v38
	v_add_f32_e32 v16, v4, v16
	v_add_f32_e32 v16, v5, v16
	s_waitcnt lgkmcnt(0)
	v_add_f32_e32 v16, v72, v16
	v_add_f32_e32 v16, v73, v16
	v_add_f32_e32 v16, v74, v16
	v_add_f32_e32 v16, v75, v16
	v_and_b32_e32 v77, 0xffff0000, v56
	v_lshlrev_b32_e32 v76, 16, v56
	v_and_b32_e32 v79, 0xffff0000, v60
	v_lshlrev_b32_e32 v78, 16, v60
	v_pk_mul_f32 v[84:85], v[76:77], v[78:79]
	s_waitcnt vmcnt(11)
	v_mov_b64 v[76:77], v[198:199]
	v_mov_b64 v[78:79], v[200:201]
	s_nop 1
	s_waitcnt vmcnt(10)
	v_mov_b64 v[80:81], v[202:203]
	v_mov_b64 v[82:83], v[204:205]
	s_nop 1
	v_lshlrev_b32_e32 v56, 16, v61
	v_lshlrev_b32_e32 v60, 16, v62
	v_lshlrev_b32_e32 v90, 16, v6
	v_lshlrev_b32_e32 v86, 16, v11
	v_and_b32_e32 v87, 0xffff0000, v11
	v_and_b32_e32 v91, 0xffff0000, v6
	v_lshlrev_b32_e32 v6, 16, v10
	v_pk_mul_f32 v[80:81], v[84:85], v[80:81]
	s_nop 0
	v_add_f32_e32 v38, 0, v80
	v_add_f32_e32 v38, v81, v38
	v_and_b32_e32 v81, 0xffff0000, v57
	v_lshlrev_b32_e32 v80, 16, v57
	v_and_b32_e32 v57, 0xffff0000, v61
	v_pk_mul_f32 v[56:57], v[80:81], v[56:57]
	v_and_b32_e32 v61, 0xffff0000, v62
	v_pk_mul_f32 v[56:57], v[56:57], v[82:83]
	v_lshlrev_b32_e32 v62, 16, v8
	v_add_f32_e32 v38, v56, v38
	v_add_f32_e32 v38, v57, v38
	v_and_b32_e32 v57, 0xffff0000, v58
	v_lshlrev_b32_e32 v56, 16, v58
	v_pk_mul_f32 v[56:57], v[56:57], v[60:61]
	v_lshlrev_b32_e32 v58, 16, v63
	v_pk_mul_f32 v[56:57], v[56:57], v[76:77]
	v_lshlrev_b32_e32 v84, 16, v7
	v_add_f32_e32 v38, v56, v38
	v_add_f32_e32 v38, v57, v38
	v_and_b32_e32 v57, 0xffff0000, v59
	v_lshlrev_b32_e32 v56, 16, v59
	v_and_b32_e32 v59, 0xffff0000, v63
	v_pk_mul_f32 v[56:57], v[56:57], v[58:59]
	v_lshlrev_b32_e32 v58, 16, v13
	v_pk_mul_f32 v[56:57], v[56:57], v[78:79]
	v_and_b32_e32 v59, 0xffff0000, v13
	v_add_f32_e32 v38, v56, v38
	v_add_f32_e32 v56, v57, v38
	ds_bpermute_b32 v38, v1, v16
	v_and_b32_e32 v57, 0xffff0000, v9
	v_and_b32_e32 v63, 0xffff0000, v8
	v_lshlrev_b32_e32 v8, 16, v12
	v_and_b32_e32 v85, 0xffff0000, v7
	s_waitcnt lgkmcnt(0)
	v_add_f32_e32 v16, v16, v38
	ds_bpermute_b32 v38, v37, v16
	v_and_b32_e32 v7, 0xffff0000, v10
	s_waitcnt lgkmcnt(0)
	v_add_f32_e32 v16, v16, v38
	ds_bpermute_b32 v38, v41, v16
	s_waitcnt lgkmcnt(0)
	v_add_f32_e32 v16, v16, v38
	v_mul_f32_e32 v38, 0x3c800000, v16
	ds_bpermute_b32 v16, v1, v56
	v_pk_add_f32 v[60:61], v[74:75], v[38:39] op_sel_hi:[1,0] neg_lo:[0,1] neg_hi:[0,1]
	v_pk_add_f32 v[2:3], v[2:3], v[38:39] op_sel_hi:[1,0] neg_lo:[0,1] neg_hi:[0,1]
	v_pk_add_f32 v[4:5], v[4:5], v[38:39] op_sel_hi:[1,0] neg_lo:[0,1] neg_hi:[0,1]
	v_pk_mul_f32 v[10:11], v[2:3], v[2:3]
	s_waitcnt lgkmcnt(0)
	v_add_f32_e32 v16, v56, v16
	ds_bpermute_b32 v56, v37, v16
	v_pk_mul_f32 v[88:89], v[4:5], v[4:5]
	v_add_f32_e32 v10, v10, v11
	v_add_f32_e32 v10, v88, v10
	v_add_f32_e32 v10, v89, v10
	s_waitcnt lgkmcnt(0)
	v_add_f32_e32 v16, v16, v56
	ds_bpermute_b32 v56, v41, v16
	v_pk_mul_f32 v[80:81], v[60:61], v[60:61]
	s_waitcnt lgkmcnt(0)
	v_add_f32_e32 v16, v16, v56
	v_lshlrev_b32_e32 v56, 16, v9
	v_and_b32_e32 v9, 0xffff0000, v12
	v_pk_add_f32 v[12:13], v[72:73], v[38:39] op_sel_hi:[1,0] neg_lo:[0,1] neg_hi:[0,1]
	s_waitcnt vmcnt(9)
	v_mov_b64 v[72:73], v[206:207]
	v_mov_b64 v[74:75], v[208:209]
	s_nop 1
	s_waitcnt vmcnt(8)
	v_mov_b64 v[76:77], v[210:211]
	v_mov_b64 v[78:79], v[212:213]
	s_nop 1
	v_pk_mul_f32 v[82:83], v[12:13], v[12:13]
	s_nop 0
	v_add_f32_e32 v10, v82, v10
	v_add_f32_e32 v10, v83, v10
	v_add_f32_e32 v10, v80, v10
	v_add_f32_e32 v10, v81, v10
	ds_bpermute_b32 v11, v1, v10
	s_waitcnt lgkmcnt(0)
	v_add_f32_e32 v10, v10, v11
	ds_bpermute_b32 v11, v37, v10
	s_waitcnt lgkmcnt(0)
	v_add_f32_e32 v10, v10, v11
	ds_bpermute_b32 v11, v41, v10
	s_waitcnt lgkmcnt(0)
	v_add_f32_e32 v10, v10, v11
	v_fmamk_f32 v10, v10, 0x3c800000, v69
	v_cmp_gt_f32_e32 vcc, s11, v10
	v_mul_f32_e32 v11, 0x4f800000, v10
	s_nop 0
	v_cndmask_b32_e32 v10, v10, v11, vcc
	v_sqrt_f32_e32 v11, v10
	s_nop 0
	v_add_u32_e32 v38, -1, v11
	v_fma_f32 v71, -v38, v11, v10
	v_cmp_ge_f32_e64 s[0:1], 0, v71
	v_add_u32_e32 v71, 1, v11
	s_nop 0
	v_cndmask_b32_e64 v38, v11, v38, s[0:1]
	v_fma_f32 v11, -v71, v11, v10
	v_cmp_lt_f32_e64 s[0:1], 0, v11
	s_nop 1
	v_cndmask_b32_e64 v11, v38, v71, s[0:1]
	v_mul_f32_e32 v38, 0x37800000, v11
	v_cndmask_b32_e32 v11, v11, v38, vcc
	v_cmp_class_f32_e32 vcc, v10, v70
	s_nop 1
	v_cndmask_b32_e32 v10, v11, v10, vcc
	v_div_scale_f32 v11, s[0:1], v10, v10, 1.0
	v_rcp_f32_e32 v38, v11
	s_nop 0
	v_fma_f32 v71, -v11, v38, 1.0
	v_fmac_f32_e32 v38, v71, v38
	v_div_scale_f32 v71, vcc, 1.0, v10, 1.0
	v_mul_f32_e32 v80, v71, v38
	v_fma_f32 v81, -v11, v80, v71
	v_fmac_f32_e32 v80, v81, v38
	v_fma_f32 v11, -v11, v80, v71
	v_div_fmas_f32 v11, v11, v38, v80
	v_div_fixup_f32 v10, v11, v10, 1.0
	v_pk_mul_f32 v[2:3], v[2:3], v[10:11] op_sel_hi:[1,0]
	v_pk_mul_f32 v[4:5], v[4:5], v[10:11] op_sel_hi:[1,0]
	v_lshlrev_b32_e32 v38, 1, v36
	v_pk_mul_f32 v[2:3], v[76:77], v[2:3]
	s_nop 0
	v_pk_fma_f32 v[2:3], v[16:17], v[90:91], v[2:3] op_sel_hi:[0,1,1]
	v_pk_mul_f32 v[2:3], v[2:3], v[6:7]
	v_pk_mul_f32 v[6:7], v[12:13], v[10:11] op_sel_hi:[1,0]
	v_pk_mul_f32 v[4:5], v[78:79], v[4:5]
	v_pk_mul_f32 v[6:7], v[72:73], v[6:7]
	v_pk_fma_f32 v[4:5], v[16:17], v[84:85], v[4:5] op_sel_hi:[0,1,1]
	v_pk_fma_f32 v[6:7], v[16:17], v[62:63], v[6:7] op_sel_hi:[0,1,1]
	v_pk_mul_f32 v[6:7], v[6:7], v[8:9]
	v_pk_mul_f32 v[8:9], v[60:61], v[10:11] op_sel_hi:[1,0]
	v_lshlrev_b64 v[10:11], 12, v[14:15]
	v_pk_mul_f32 v[8:9], v[74:75], v[8:9]
	v_lshl_add_u64 v[10:11], v[22:23], 0, v[10:11]
	v_pk_fma_f32 v[8:9], v[16:17], v[56:57], v[8:9] op_sel_hi:[0,1,1]
	v_pk_mul_f32 v[4:5], v[4:5], v[86:87]
	v_pk_mul_f32 v[8:9], v[8:9], v[58:59]
	v_lshl_add_u64 v[10:11], v[10:11], 0, s[4:5]
	v_lshl_add_u64 v[10:11], v[10:11], 0, v[38:39]
	v_cvt_pk_bf16_f32 v2, v2, v3
	v_cvt_pk_bf16_f32 v3, v4, v5
	v_cvt_pk_bf16_f32 v4, v6, v7
	v_cvt_pk_bf16_f32 v5, v8, v9
	global_store_dwordx4 v[10:11], v[2:5], off offset:1024
	v_mov_b32_e32 v137, s14
	v_or_b32_e32 v136, s13, v46
	v_lshlrev_b64 v[136:137], 9, v[136:137]
	v_or_b32_e32 v136, v136, v36
	v_or_b32_e32 v136, s12, v136
	v_lshlrev_b64 v[136:137], 1, v[136:137]
	v_lshl_add_u64 v[138:139], v[24:25], 0, v[136:137]
	global_load_dwordx4 v[150:153], v[138:139], off
	v_lshl_add_u64 v[138:139], v[26:27], 0, v[136:137]
	global_load_dwordx4 v[154:157], v[138:139], off
	v_lshl_add_u64 v[138:139], v[28:29], 0, v[136:137]
	global_load_dwordx4 v[158:161], v[138:139], off
	v_lshl_add_u64 v[138:139], v[30:31], 0, v[136:137]
	global_load_dwordx4 v[162:165], v[138:139], off
	s_nop 1
	v_mov_b32_e32 v3, s14
	v_or_b32_e32 v2, s13, v42
	v_lshlrev_b64 v[12:13], 9, v[2:3]
	v_or_b32_e32 v4, v12, v36
	v_or_b32_e32 v12, s12, v4
	v_lshlrev_b64 v[72:73], 1, v[12:13]
	v_lshl_add_u64 v[12:13], v[24:25], 0, v[72:73]
	v_lshl_add_u64 v[56:57], v[26:27], 0, v[72:73]
	ds_read_b128 v[4:7], v68 offset:2176
	ds_read_b128 v[8:11], v68 offset:2192
	s_waitcnt vmcnt(12)
	v_mov_b64 v[12:13], v[166:167]
	v_mov_b64 v[14:15], v[168:169]
	s_nop 1
	v_lshl_add_u64 v[60:61], v[28:29], 0, v[72:73]
	s_waitcnt vmcnt(11)
	v_mov_b64 v[56:57], v[170:171]
	v_mov_b64 v[58:59], v[172:173]
	s_nop 1
	v_lshl_add_u64 v[72:73], v[30:31], 0, v[72:73]
	s_waitcnt vmcnt(10)
	v_mov_b64 v[60:61], v[174:175]
	v_mov_b64 v[62:63], v[176:177]
	s_nop 1
	s_waitcnt lgkmcnt(1)
	v_add_f32_e32 v16, 0, v4
	s_waitcnt vmcnt(9)
	v_mov_b64 v[72:73], v[178:179]
	v_mov_b64 v[74:75], v[180:181]
	s_nop 1
	v_add_f32_e32 v16, v5, v16
	v_lshlrev_b64 v[2:3], 12, v[2:3]
	v_lshl_add_u64 v[2:3], v[22:23], 0, v[2:3]
	v_lshl_add_u64 v[2:3], v[2:3], 0, s[4:5]
	v_and_b32_e32 v77, 0xffff0000, v12
	v_lshlrev_b32_e32 v76, 16, v12
	v_and_b32_e32 v79, 0xffff0000, v56
	v_lshlrev_b32_e32 v78, 16, v56
	v_pk_mul_f32 v[84:85], v[76:77], v[78:79]
	v_mov_b64 v[76:77], v[198:199]
	v_mov_b64 v[78:79], v[200:201]
	s_nop 1
	v_mov_b64 v[80:81], v[202:203]
	v_mov_b64 v[82:83], v[204:205]
	s_nop 1
	v_lshlrev_b32_e32 v86, 16, v61
	v_and_b32_e32 v87, 0xffff0000, v61
	v_lshlrev_b32_e32 v88, 16, v73
	v_and_b32_e32 v89, 0xffff0000, v73
	v_lshlrev_b32_e32 v92, 16, v60
	v_and_b32_e32 v93, 0xffff0000, v60
	v_lshlrev_b32_e32 v60, 16, v72
	v_and_b32_e32 v61, 0xffff0000, v72
	v_pk_mul_f32 v[80:81], v[84:85], v[80:81]
	s_nop 0
	v_add_f32_e32 v12, 0, v80
	v_add_f32_e32 v56, v81, v12
	v_add_f32_e32 v12, v6, v16
	v_add_f32_e32 v16, v7, v12
	v_and_b32_e32 v81, 0xffff0000, v13
	v_lshlrev_b32_e32 v80, 16, v13
	v_and_b32_e32 v13, 0xffff0000, v57
	v_lshlrev_b32_e32 v12, 16, v57
	v_pk_mul_f32 v[12:13], v[80:81], v[12:13]
	v_and_b32_e32 v57, 0xffff0000, v58
	v_pk_mul_f32 v[12:13], v[12:13], v[82:83]
	v_lshlrev_b32_e32 v82, 16, v62
	v_add_f32_e32 v12, v12, v56
	v_add_f32_e32 v71, v13, v12
	s_waitcnt lgkmcnt(0)
	v_add_f32_e32 v12, v8, v16
	v_add_f32_e32 v16, v9, v12
	v_and_b32_e32 v13, 0xffff0000, v14
	v_lshlrev_b32_e32 v12, 16, v14
	v_lshlrev_b32_e32 v56, 16, v58
	v_pk_mul_f32 v[12:13], v[12:13], v[56:57]
	v_lshlrev_b32_e32 v14, 16, v59
	v_pk_mul_f32 v[12:13], v[12:13], v[76:77]
	v_lshlrev_b32_e32 v58, 16, v63
	v_add_f32_e32 v12, v12, v71
	v_add_f32_e32 v56, v13, v12
	v_add_f32_e32 v12, v10, v16
	v_add_f32_e32 v16, v11, v12
	v_and_b32_e32 v13, 0xffff0000, v15
	v_lshlrev_b32_e32 v12, 16, v15
	v_and_b32_e32 v15, 0xffff0000, v59
	v_pk_mul_f32 v[12:13], v[12:13], v[14:15]
	v_and_b32_e32 v59, 0xffff0000, v63
	v_pk_mul_f32 v[12:13], v[12:13], v[78:79]
	v_lshlrev_b32_e32 v76, 16, v75
	v_add_f32_e32 v12, v12, v56
	v_add_f32_e32 v12, v13, v12
	ds_bpermute_b32 v13, v1, v16
	v_and_b32_e32 v77, 0xffff0000, v75
	v_and_b32_e32 v83, 0xffff0000, v62
	v_lshlrev_b32_e32 v62, 16, v74
	v_and_b32_e32 v63, 0xffff0000, v74
	s_waitcnt lgkmcnt(0)
	v_add_f32_e32 v13, v16, v13
	ds_bpermute_b32 v14, v37, v13
	s_waitcnt lgkmcnt(0)
	v_add_f32_e32 v13, v13, v14
	ds_bpermute_b32 v14, v41, v13
	s_waitcnt lgkmcnt(0)
	v_add_f32_e32 v13, v13, v14
	v_mul_f32_e32 v16, 0x3c800000, v13
	ds_bpermute_b32 v13, v1, v12
	v_pk_add_f32 v[78:79], v[10:11], v[16:17] op_sel_hi:[1,0] neg_lo:[0,1] neg_hi:[0,1]
	v_pk_add_f32 v[74:75], v[8:9], v[16:17] op_sel_hi:[1,0] neg_lo:[0,1] neg_hi:[0,1]
	v_pk_add_f32 v[4:5], v[4:5], v[16:17] op_sel_hi:[1,0] neg_lo:[0,1] neg_hi:[0,1]
	v_pk_add_f32 v[6:7], v[6:7], v[16:17] op_sel_hi:[1,0] neg_lo:[0,1] neg_hi:[0,1]
	s_waitcnt lgkmcnt(0)
	v_add_f32_e32 v12, v12, v13
	ds_bpermute_b32 v13, v37, v12
	v_pk_mul_f32 v[72:73], v[4:5], v[4:5]
	v_pk_mul_f32 v[90:91], v[6:7], v[6:7]
	v_add_f32_e32 v16, v72, v73
	v_add_f32_e32 v16, v90, v16
	s_waitcnt lgkmcnt(0)
	v_add_f32_e32 v12, v12, v13
	ds_bpermute_b32 v13, v41, v12
	v_pk_mul_f32 v[84:85], v[74:75], v[74:75]
	v_add_f32_e32 v16, v91, v16
	v_add_f32_e32 v16, v84, v16
	v_pk_mul_f32 v[80:81], v[78:79], v[78:79]
	s_waitcnt lgkmcnt(0)
	v_add_f32_e32 v56, v12, v13
	v_mov_b64 v[8:9], v[206:207]
	v_mov_b64 v[10:11], v[208:209]
	s_nop 1
	v_mov_b64 v[12:13], v[210:211]
	v_mov_b64 v[14:15], v[212:213]
	s_nop 1
	v_add_f32_e32 v16, v85, v16
	v_add_f32_e32 v16, v80, v16
	v_add_f32_e32 v16, v81, v16
	ds_bpermute_b32 v57, v1, v16
	s_waitcnt lgkmcnt(0)
	v_add_f32_e32 v16, v16, v57
	ds_bpermute_b32 v57, v37, v16
	s_waitcnt lgkmcnt(0)
	v_add_f32_e32 v16, v16, v57
	ds_bpermute_b32 v57, v41, v16
	s_waitcnt lgkmcnt(0)
	v_add_f32_e32 v16, v16, v57
	v_fmamk_f32 v16, v16, 0x3c800000, v69
	v_cmp_gt_f32_e32 vcc, s11, v16
	v_mul_f32_e32 v57, 0x4f800000, v16
	s_nop 0
	v_cndmask_b32_e32 v16, v16, v57, vcc
	v_sqrt_f32_e32 v57, v16
	s_nop 0
	v_add_u32_e32 v71, -1, v57
	v_fma_f32 v72, -v71, v57, v16
	v_cmp_ge_f32_e64 s[0:1], 0, v72
	v_add_u32_e32 v72, 1, v57
	s_nop 0
	v_cndmask_b32_e64 v71, v57, v71, s[0:1]
	v_fma_f32 v57, -v72, v57, v16
	v_cmp_lt_f32_e64 s[0:1], 0, v57
	s_nop 1
	v_cndmask_b32_e64 v57, v71, v72, s[0:1]
	v_mul_f32_e32 v71, 0x37800000, v57
	v_cndmask_b32_e32 v57, v57, v71, vcc
	v_cmp_class_f32_e32 vcc, v16, v70
	s_nop 1
	v_cndmask_b32_e32 v16, v57, v16, vcc
	v_div_scale_f32 v57, s[0:1], v16, v16, 1.0
	v_rcp_f32_e32 v71, v57
	s_nop 0
	v_fma_f32 v72, -v57, v71, 1.0
	v_fmac_f32_e32 v71, v72, v71
	v_div_scale_f32 v72, vcc, 1.0, v16, 1.0
	v_mul_f32_e32 v73, v72, v71
	v_fma_f32 v80, -v57, v73, v72
	v_fmac_f32_e32 v73, v80, v71
	v_fma_f32 v57, -v57, v73, v72
	v_div_fmas_f32 v57, v57, v71, v73
	v_div_fixup_f32 v16, v57, v16, 1.0
	v_pk_mul_f32 v[4:5], v[4:5], v[16:17] op_sel_hi:[1,0]
	v_pk_mul_f32 v[6:7], v[6:7], v[16:17] op_sel_hi:[1,0]
	v_pk_mul_f32 v[4:5], v[12:13], v[4:5]
	v_pk_mul_f32 v[12:13], v[74:75], v[16:17] op_sel_hi:[1,0]
	v_pk_mul_f32 v[6:7], v[14:15], v[6:7]
	v_pk_mul_f32 v[8:9], v[8:9], v[12:13]
	v_pk_mul_f32 v[12:13], v[78:79], v[16:17] op_sel_hi:[1,0]
	v_pk_fma_f32 v[4:5], v[56:57], v[92:93], v[4:5] op_sel_hi:[0,1,1]
	v_pk_mul_f32 v[10:11], v[10:11], v[12:13]
	v_pk_fma_f32 v[6:7], v[56:57], v[86:87], v[6:7] op_sel_hi:[0,1,1]
	v_pk_fma_f32 v[8:9], v[56:57], v[82:83], v[8:9] op_sel_hi:[0,1,1]
	v_pk_fma_f32 v[10:11], v[56:57], v[58:59], v[10:11] op_sel_hi:[0,1,1]
	v_pk_mul_f32 v[4:5], v[4:5], v[60:61]
	v_pk_mul_f32 v[6:7], v[6:7], v[88:89]
	v_pk_mul_f32 v[8:9], v[8:9], v[62:63]
	v_pk_mul_f32 v[10:11], v[10:11], v[76:77]
	v_lshl_add_u64 v[12:13], v[2:3], 0, v[38:39]
	v_cvt_pk_bf16_f32 v2, v4, v5
	v_cvt_pk_bf16_f32 v3, v6, v7
	v_cvt_pk_bf16_f32 v4, v8, v9
	v_cvt_pk_bf16_f32 v5, v10, v11
	global_store_dwordx4 v[12:13], v[2:5], off offset:1024
	s_nop 1
	v_mov_b32_e32 v3, s14
	v_or_b32_e32 v2, s13, v44
	v_lshlrev_b64 v[12:13], 9, v[2:3]
	v_or_b32_e32 v4, v12, v36
	v_or_b32_e32 v12, s12, v4
	v_lshlrev_b64 v[72:73], 1, v[12:13]
	v_lshl_add_u64 v[12:13], v[24:25], 0, v[72:73]
	v_lshl_add_u64 v[56:57], v[26:27], 0, v[72:73]
	ds_read_b128 v[4:7], v68 offset:4352
	ds_read_b128 v[8:11], v68 offset:4368
	s_waitcnt vmcnt(9)
	v_mov_b64 v[12:13], v[182:183]
	v_mov_b64 v[14:15], v[184:185]
	s_nop 1
	v_lshl_add_u64 v[60:61], v[28:29], 0, v[72:73]
	s_waitcnt vmcnt(8)
	v_mov_b64 v[56:57], v[186:187]
	v_mov_b64 v[58:59], v[188:189]
	s_nop 1
	v_lshl_add_u64 v[72:73], v[30:31], 0, v[72:73]
	s_waitcnt vmcnt(7)
	v_mov_b64 v[60:61], v[190:191]
	v_mov_b64 v[62:63], v[192:193]
	s_nop 1
	s_waitcnt lgkmcnt(1)
	v_add_f32_e32 v16, 0, v4
	s_waitcnt vmcnt(6)
	v_mov_b64 v[72:73], v[194:195]
	v_mov_b64 v[74:75], v[196:197]
	s_nop 1
	v_add_f32_e32 v16, v5, v16
	v_lshlrev_b64 v[2:3], 12, v[2:3]
	v_lshl_add_u64 v[2:3], v[22:23], 0, v[2:3]
	v_lshl_add_u64 v[2:3], v[2:3], 0, s[4:5]
	v_and_b32_e32 v77, 0xffff0000, v12
	v_lshlrev_b32_e32 v76, 16, v12
	v_and_b32_e32 v79, 0xffff0000, v56
	v_lshlrev_b32_e32 v78, 16, v56
	v_pk_mul_f32 v[84:85], v[76:77], v[78:79]
	v_mov_b64 v[76:77], v[198:199]
	v_mov_b64 v[78:79], v[200:201]
	s_nop 1
	v_mov_b64 v[80:81], v[202:203]
	v_mov_b64 v[82:83], v[204:205]
	s_nop 1
	v_lshlrev_b32_e32 v86, 16, v61
	v_and_b32_e32 v87, 0xffff0000, v61
	v_lshlrev_b32_e32 v88, 16, v73
	v_and_b32_e32 v89, 0xffff0000, v73
	v_lshlrev_b32_e32 v92, 16, v60
	v_and_b32_e32 v93, 0xffff0000, v60
	v_lshlrev_b32_e32 v60, 16, v72
	v_and_b32_e32 v61, 0xffff0000, v72
	v_pk_mul_f32 v[80:81], v[84:85], v[80:81]
	s_nop 0
	v_add_f32_e32 v12, 0, v80
	v_add_f32_e32 v56, v81, v12
	v_add_f32_e32 v12, v6, v16
	v_add_f32_e32 v16, v7, v12
	v_and_b32_e32 v81, 0xffff0000, v13
	v_lshlrev_b32_e32 v80, 16, v13
	v_and_b32_e32 v13, 0xffff0000, v57
	v_lshlrev_b32_e32 v12, 16, v57
	v_pk_mul_f32 v[12:13], v[80:81], v[12:13]
	v_and_b32_e32 v57, 0xffff0000, v58
	v_pk_mul_f32 v[12:13], v[12:13], v[82:83]
	v_lshlrev_b32_e32 v82, 16, v62
	v_add_f32_e32 v12, v12, v56
	v_add_f32_e32 v71, v13, v12
	s_waitcnt lgkmcnt(0)
	v_add_f32_e32 v12, v8, v16
	v_add_f32_e32 v16, v9, v12
	v_and_b32_e32 v13, 0xffff0000, v14
	v_lshlrev_b32_e32 v12, 16, v14
	v_lshlrev_b32_e32 v56, 16, v58
	v_pk_mul_f32 v[12:13], v[12:13], v[56:57]
	v_lshlrev_b32_e32 v14, 16, v59
	v_pk_mul_f32 v[12:13], v[12:13], v[76:77]
	v_lshlrev_b32_e32 v58, 16, v63
	v_add_f32_e32 v12, v12, v71
	v_add_f32_e32 v56, v13, v12
	v_add_f32_e32 v12, v10, v16
	v_add_f32_e32 v16, v11, v12
	v_and_b32_e32 v13, 0xffff0000, v15
	v_lshlrev_b32_e32 v12, 16, v15
	v_and_b32_e32 v15, 0xffff0000, v59
	v_pk_mul_f32 v[12:13], v[12:13], v[14:15]
	v_and_b32_e32 v59, 0xffff0000, v63
	v_pk_mul_f32 v[12:13], v[12:13], v[78:79]
	v_lshlrev_b32_e32 v76, 16, v75
	v_add_f32_e32 v12, v12, v56
	v_add_f32_e32 v12, v13, v12
	ds_bpermute_b32 v13, v1, v16
	v_and_b32_e32 v77, 0xffff0000, v75
	v_and_b32_e32 v83, 0xffff0000, v62
	v_lshlrev_b32_e32 v62, 16, v74
	v_and_b32_e32 v63, 0xffff0000, v74
	s_waitcnt lgkmcnt(0)
	v_add_f32_e32 v13, v16, v13
	ds_bpermute_b32 v14, v37, v13
	s_waitcnt lgkmcnt(0)
	v_add_f32_e32 v13, v13, v14
	ds_bpermute_b32 v14, v41, v13
	s_waitcnt lgkmcnt(0)
	v_add_f32_e32 v13, v13, v14
	v_mul_f32_e32 v16, 0x3c800000, v13
	ds_bpermute_b32 v13, v1, v12
	v_pk_add_f32 v[78:79], v[10:11], v[16:17] op_sel_hi:[1,0] neg_lo:[0,1] neg_hi:[0,1]
	v_pk_add_f32 v[74:75], v[8:9], v[16:17] op_sel_hi:[1,0] neg_lo:[0,1] neg_hi:[0,1]
	v_pk_add_f32 v[4:5], v[4:5], v[16:17] op_sel_hi:[1,0] neg_lo:[0,1] neg_hi:[0,1]
	v_pk_add_f32 v[6:7], v[6:7], v[16:17] op_sel_hi:[1,0] neg_lo:[0,1] neg_hi:[0,1]
	s_waitcnt lgkmcnt(0)
	v_add_f32_e32 v12, v12, v13
	ds_bpermute_b32 v13, v37, v12
	v_pk_mul_f32 v[72:73], v[4:5], v[4:5]
	v_pk_mul_f32 v[90:91], v[6:7], v[6:7]
	v_add_f32_e32 v16, v72, v73
	v_add_f32_e32 v16, v90, v16
	s_waitcnt lgkmcnt(0)
	v_add_f32_e32 v12, v12, v13
	ds_bpermute_b32 v13, v41, v12
	v_pk_mul_f32 v[84:85], v[74:75], v[74:75]
	v_add_f32_e32 v16, v91, v16
	v_add_f32_e32 v16, v84, v16
	v_pk_mul_f32 v[80:81], v[78:79], v[78:79]
	s_waitcnt lgkmcnt(0)
	v_add_f32_e32 v56, v12, v13
	v_mov_b64 v[8:9], v[206:207]
	v_mov_b64 v[10:11], v[208:209]
	s_nop 1
	v_mov_b64 v[12:13], v[210:211]
	v_mov_b64 v[14:15], v[212:213]
	s_nop 1
	v_add_f32_e32 v16, v85, v16
	v_add_f32_e32 v16, v80, v16
	v_add_f32_e32 v16, v81, v16
	ds_bpermute_b32 v57, v1, v16
	s_waitcnt lgkmcnt(0)
	v_add_f32_e32 v16, v16, v57
	ds_bpermute_b32 v57, v37, v16
	s_waitcnt lgkmcnt(0)
	v_add_f32_e32 v16, v16, v57
	ds_bpermute_b32 v57, v41, v16
	s_waitcnt lgkmcnt(0)
	v_add_f32_e32 v16, v16, v57
	v_fmamk_f32 v16, v16, 0x3c800000, v69
	v_cmp_gt_f32_e32 vcc, s11, v16
	v_mul_f32_e32 v57, 0x4f800000, v16
	s_nop 0
	v_cndmask_b32_e32 v16, v16, v57, vcc
	v_sqrt_f32_e32 v57, v16
	s_nop 0
	v_add_u32_e32 v71, -1, v57
	v_fma_f32 v72, -v71, v57, v16
	v_cmp_ge_f32_e64 s[0:1], 0, v72
	v_add_u32_e32 v72, 1, v57
	s_nop 0
	v_cndmask_b32_e64 v71, v57, v71, s[0:1]
	v_fma_f32 v57, -v72, v57, v16
	v_cmp_lt_f32_e64 s[0:1], 0, v57
	s_nop 1
	v_cndmask_b32_e64 v57, v71, v72, s[0:1]
	v_mul_f32_e32 v71, 0x37800000, v57
	v_cndmask_b32_e32 v57, v57, v71, vcc
	v_cmp_class_f32_e32 vcc, v16, v70
	s_nop 1
	v_cndmask_b32_e32 v16, v57, v16, vcc
	v_div_scale_f32 v57, s[0:1], v16, v16, 1.0
	v_rcp_f32_e32 v71, v57
	s_nop 0
	v_fma_f32 v72, -v57, v71, 1.0
	v_fmac_f32_e32 v71, v72, v71
	v_div_scale_f32 v72, vcc, 1.0, v16, 1.0
	v_mul_f32_e32 v73, v72, v71
	v_fma_f32 v80, -v57, v73, v72
	v_fmac_f32_e32 v73, v80, v71
	v_fma_f32 v57, -v57, v73, v72
	v_div_fmas_f32 v57, v57, v71, v73
	v_div_fixup_f32 v16, v57, v16, 1.0
	v_pk_mul_f32 v[4:5], v[4:5], v[16:17] op_sel_hi:[1,0]
	v_pk_mul_f32 v[6:7], v[6:7], v[16:17] op_sel_hi:[1,0]
	v_pk_mul_f32 v[4:5], v[12:13], v[4:5]
	v_pk_mul_f32 v[12:13], v[74:75], v[16:17] op_sel_hi:[1,0]
	v_pk_mul_f32 v[6:7], v[14:15], v[6:7]
	v_pk_mul_f32 v[8:9], v[8:9], v[12:13]
	v_pk_mul_f32 v[12:13], v[78:79], v[16:17] op_sel_hi:[1,0]
	v_pk_fma_f32 v[4:5], v[56:57], v[92:93], v[4:5] op_sel_hi:[0,1,1]
	v_pk_mul_f32 v[10:11], v[10:11], v[12:13]
	v_pk_fma_f32 v[6:7], v[56:57], v[86:87], v[6:7] op_sel_hi:[0,1,1]
	v_pk_fma_f32 v[8:9], v[56:57], v[82:83], v[8:9] op_sel_hi:[0,1,1]
	v_pk_fma_f32 v[10:11], v[56:57], v[58:59], v[10:11] op_sel_hi:[0,1,1]
	v_pk_mul_f32 v[4:5], v[4:5], v[60:61]
	v_pk_mul_f32 v[6:7], v[6:7], v[88:89]
	v_pk_mul_f32 v[8:9], v[8:9], v[62:63]
	v_pk_mul_f32 v[10:11], v[10:11], v[76:77]
	v_lshl_add_u64 v[12:13], v[2:3], 0, v[38:39]
	v_cvt_pk_bf16_f32 v2, v4, v5
	v_cvt_pk_bf16_f32 v3, v6, v7
	v_cvt_pk_bf16_f32 v4, v8, v9
	v_cvt_pk_bf16_f32 v5, v10, v11
	v_mov_b32_e32 v11, s14
	v_or_b32_e32 v10, s13, v46
	global_store_dwordx4 v[12:13], v[2:5], off offset:1024
	v_lshlrev_b64 v[12:13], 9, v[10:11]
	v_lshlrev_b64 v[10:11], 12, v[10:11]
	v_or_b32_e32 v2, v12, v36
	v_or_b32_e32 v12, s12, v2
	v_lshlrev_b64 v[72:73], 1, v[12:13]
	v_lshl_add_u64 v[12:13], v[24:25], 0, v[72:73]
	v_lshl_add_u64 v[56:57], v[26:27], 0, v[72:73]
	ds_read_b128 v[2:5], v68 offset:6528
	ds_read_b128 v[6:9], v68 offset:6544
	s_waitcnt vmcnt(5)
	v_mov_b64 v[12:13], v[150:151]
	v_mov_b64 v[14:15], v[152:153]
	s_nop 1
	v_lshl_add_u64 v[60:61], v[28:29], 0, v[72:73]
	s_waitcnt vmcnt(4)
	v_mov_b64 v[56:57], v[154:155]
	v_mov_b64 v[58:59], v[156:157]
	s_nop 1
	v_lshl_add_u64 v[72:73], v[30:31], 0, v[72:73]
	s_waitcnt vmcnt(3)
	v_mov_b64 v[60:61], v[158:159]
	v_mov_b64 v[62:63], v[160:161]
	s_nop 1
	s_waitcnt lgkmcnt(1)
	v_add_f32_e32 v16, 0, v2
	s_waitcnt vmcnt(2)
	v_mov_b64 v[72:73], v[162:163]
	v_mov_b64 v[74:75], v[164:165]
	s_nop 1
	v_add_f32_e32 v16, v3, v16
	v_lshl_add_u64 v[10:11], v[22:23], 0, v[10:11]
	v_lshl_add_u64 v[10:11], v[10:11], 0, s[4:5]
	v_lshl_add_u64 v[10:11], v[10:11], 0, v[38:39]
	v_and_b32_e32 v77, 0xffff0000, v12
	v_lshlrev_b32_e32 v76, 16, v12
	v_and_b32_e32 v79, 0xffff0000, v56
	v_lshlrev_b32_e32 v78, 16, v56
	v_pk_mul_f32 v[84:85], v[76:77], v[78:79]
	v_mov_b64 v[76:77], v[198:199]
	v_mov_b64 v[78:79], v[200:201]
	s_nop 1
	v_mov_b64 v[80:81], v[202:203]
	v_mov_b64 v[82:83], v[204:205]
	s_nop 1
	v_lshlrev_b32_e32 v86, 16, v61
	v_and_b32_e32 v87, 0xffff0000, v61
	v_lshlrev_b32_e32 v92, 16, v60
	v_and_b32_e32 v93, 0xffff0000, v60
	v_lshlrev_b32_e32 v60, 16, v72
	v_and_b32_e32 v61, 0xffff0000, v72
	v_lshlrev_b32_e32 v88, 16, v73
	v_and_b32_e32 v89, 0xffff0000, v73
	v_pk_mul_f32 v[80:81], v[84:85], v[80:81]
	s_nop 0
	v_add_f32_e32 v12, 0, v80
	v_add_f32_e32 v56, v81, v12
	v_add_f32_e32 v12, v4, v16
	v_add_f32_e32 v16, v5, v12
	v_and_b32_e32 v81, 0xffff0000, v13
	v_lshlrev_b32_e32 v80, 16, v13
	v_and_b32_e32 v13, 0xffff0000, v57
	v_lshlrev_b32_e32 v12, 16, v57
	v_pk_mul_f32 v[12:13], v[80:81], v[12:13]
	v_and_b32_e32 v57, 0xffff0000, v58
	v_pk_mul_f32 v[12:13], v[12:13], v[82:83]
	v_lshlrev_b32_e32 v82, 16, v62
	v_add_f32_e32 v12, v12, v56
	v_add_f32_e32 v71, v13, v12
	s_waitcnt lgkmcnt(0)
	v_add_f32_e32 v12, v6, v16
	v_add_f32_e32 v16, v7, v12
	v_and_b32_e32 v13, 0xffff0000, v14
	v_lshlrev_b32_e32 v12, 16, v14
	v_lshlrev_b32_e32 v56, 16, v58
	v_pk_mul_f32 v[12:13], v[12:13], v[56:57]
	v_lshlrev_b32_e32 v14, 16, v59
	v_pk_mul_f32 v[12:13], v[12:13], v[76:77]
	v_lshlrev_b32_e32 v58, 16, v63
	v_add_f32_e32 v12, v12, v71
	v_add_f32_e32 v56, v13, v12
	v_add_f32_e32 v12, v8, v16
	v_add_f32_e32 v16, v9, v12
	v_and_b32_e32 v13, 0xffff0000, v15
	v_lshlrev_b32_e32 v12, 16, v15
	v_and_b32_e32 v15, 0xffff0000, v59
	v_pk_mul_f32 v[12:13], v[12:13], v[14:15]
	v_and_b32_e32 v59, 0xffff0000, v63
	v_pk_mul_f32 v[12:13], v[12:13], v[78:79]
	v_lshlrev_b32_e32 v76, 16, v75
	v_add_f32_e32 v12, v12, v56
	v_add_f32_e32 v12, v13, v12
	ds_bpermute_b32 v13, v1, v16
	v_and_b32_e32 v77, 0xffff0000, v75
	v_and_b32_e32 v83, 0xffff0000, v62
	v_lshlrev_b32_e32 v62, 16, v74
	v_and_b32_e32 v63, 0xffff0000, v74
	s_waitcnt lgkmcnt(0)
	v_add_f32_e32 v13, v16, v13
	ds_bpermute_b32 v14, v37, v13
	s_waitcnt lgkmcnt(0)
	v_add_f32_e32 v13, v13, v14
	ds_bpermute_b32 v14, v41, v13
	s_waitcnt lgkmcnt(0)
	v_add_f32_e32 v13, v13, v14
	v_mul_f32_e32 v16, 0x3c800000, v13
	ds_bpermute_b32 v13, v1, v12
	v_pk_add_f32 v[78:79], v[8:9], v[16:17] op_sel_hi:[1,0] neg_lo:[0,1] neg_hi:[0,1]
	v_pk_add_f32 v[74:75], v[6:7], v[16:17] op_sel_hi:[1,0] neg_lo:[0,1] neg_hi:[0,1]
	v_pk_add_f32 v[2:3], v[2:3], v[16:17] op_sel_hi:[1,0] neg_lo:[0,1] neg_hi:[0,1]
	v_pk_add_f32 v[4:5], v[4:5], v[16:17] op_sel_hi:[1,0] neg_lo:[0,1] neg_hi:[0,1]
	s_waitcnt lgkmcnt(0)
	v_add_f32_e32 v12, v12, v13
	ds_bpermute_b32 v13, v37, v12
	v_pk_mul_f32 v[90:91], v[4:5], v[4:5]
	v_pk_mul_f32 v[84:85], v[74:75], v[74:75]
	v_pk_mul_f32 v[80:81], v[78:79], v[78:79]
	s_waitcnt lgkmcnt(0)
	v_add_f32_e32 v12, v12, v13
	ds_bpermute_b32 v13, v41, v12
	s_waitcnt lgkmcnt(0)
	v_add_f32_e32 v56, v12, v13
	v_mov_b64 v[6:7], v[206:207]
	v_mov_b64 v[8:9], v[208:209]
	s_nop 1
	v_mov_b64 v[12:13], v[210:211]
	v_mov_b64 v[14:15], v[212:213]
	s_nop 1
	v_pk_mul_f32 v[16:17], v[2:3], v[2:3]
	s_nop 0
	v_add_f32_e32 v16, v16, v17
	v_add_f32_e32 v16, v90, v16
	v_add_f32_e32 v16, v91, v16
	v_add_f32_e32 v16, v84, v16
	v_add_f32_e32 v16, v85, v16
	v_add_f32_e32 v16, v80, v16
	v_add_f32_e32 v16, v81, v16
	ds_bpermute_b32 v17, v1, v16
	s_waitcnt lgkmcnt(0)
	v_add_f32_e32 v16, v16, v17
	ds_bpermute_b32 v17, v37, v16
	s_waitcnt lgkmcnt(0)
	v_add_f32_e32 v16, v16, v17
	ds_bpermute_b32 v17, v41, v16
	s_waitcnt lgkmcnt(0)
	v_add_f32_e32 v16, v16, v17
	v_fmamk_f32 v16, v16, 0x3c800000, v69
	v_cmp_gt_f32_e32 vcc, s11, v16
	v_mul_f32_e32 v17, 0x4f800000, v16
	s_nop 0
	v_cndmask_b32_e32 v16, v16, v17, vcc
	v_sqrt_f32_e32 v17, v16
	s_nop 0
	v_add_u32_e32 v57, -1, v17
	v_fma_f32 v71, -v57, v17, v16
	v_cmp_ge_f32_e64 s[0:1], 0, v71
	v_add_u32_e32 v71, 1, v17
	s_nop 0
	v_cndmask_b32_e64 v57, v17, v57, s[0:1]
	v_fma_f32 v17, -v71, v17, v16
	v_cmp_lt_f32_e64 s[0:1], 0, v17
	s_nop 1
	v_cndmask_b32_e64 v17, v57, v71, s[0:1]
	v_mul_f32_e32 v57, 0x37800000, v17
	v_cndmask_b32_e32 v17, v17, v57, vcc
	v_cmp_class_f32_e32 vcc, v16, v70
	s_nop 1
	v_cndmask_b32_e32 v16, v17, v16, vcc
	v_div_scale_f32 v17, s[0:1], v16, v16, 1.0
	v_rcp_f32_e32 v57, v17
	s_nop 0
	v_fma_f32 v71, -v17, v57, 1.0
	v_fmac_f32_e32 v57, v71, v57
	v_div_scale_f32 v71, vcc, 1.0, v16, 1.0
	v_mul_f32_e32 v72, v71, v57
	v_fma_f32 v73, -v17, v72, v71
	v_fmac_f32_e32 v72, v73, v57
	v_fma_f32 v17, -v17, v72, v71
	v_div_fmas_f32 v17, v17, v57, v72
	v_div_fixup_f32 v16, v17, v16, 1.0
	v_pk_mul_f32 v[2:3], v[2:3], v[16:17] op_sel_hi:[1,0]
	v_pk_mul_f32 v[4:5], v[4:5], v[16:17] op_sel_hi:[1,0]
	v_pk_mul_f32 v[2:3], v[12:13], v[2:3]
	v_pk_mul_f32 v[12:13], v[74:75], v[16:17] op_sel_hi:[1,0]
	v_pk_mul_f32 v[4:5], v[14:15], v[4:5]
	v_pk_mul_f32 v[6:7], v[6:7], v[12:13]
	v_pk_mul_f32 v[12:13], v[78:79], v[16:17] op_sel_hi:[1,0]
	v_pk_fma_f32 v[2:3], v[56:57], v[92:93], v[2:3] op_sel_hi:[0,1,1]
	v_pk_mul_f32 v[8:9], v[8:9], v[12:13]
	v_pk_fma_f32 v[4:5], v[56:57], v[86:87], v[4:5] op_sel_hi:[0,1,1]
	v_pk_fma_f32 v[6:7], v[56:57], v[82:83], v[6:7] op_sel_hi:[0,1,1]
	v_pk_fma_f32 v[8:9], v[56:57], v[58:59], v[8:9] op_sel_hi:[0,1,1]
	v_pk_mul_f32 v[2:3], v[2:3], v[60:61]
	v_pk_mul_f32 v[4:5], v[4:5], v[88:89]
	v_pk_mul_f32 v[6:7], v[6:7], v[62:63]
	v_pk_mul_f32 v[8:9], v[8:9], v[76:77]
	v_cvt_pk_bf16_f32 v2, v2, v3
	v_cvt_pk_bf16_f32 v3, v4, v5
	v_cvt_pk_bf16_f32 v4, v6, v7
	v_cvt_pk_bf16_f32 v5, v8, v9
	global_store_dwordx4 v[10:11], v[2:5], off offset:1024
	s_waitcnt lgkmcnt(0)
	s_cbranch_scc1 .LBB0_1417
